# row-step table read hoist also in the layer-1 int8 QKV GEMM epilogue (spare VGPRs v228-233)
# baseline (speedup 1.0000x reference)
; __device__ __forceinline__ f32x4 i32bits_to_f32(f32x4 v) { return (f32x4){(float)__float_as_int(v.x), (float)__float_as_int(v.y), (float)__float_as_int(v.z), (float)__float_as_int(v.w)}; }
;     __device__ __forceinline__ void operator()(const f32x4 (&acc)[2][2][4][2], const Unit& u, int wr, int wc, int fr, int fq) const {
;         const int row0 = u.pm * BM + wr * 64 + fr, colt = u.pn * BM, cl = wc * 32 + 8 * fq; const int sl = IN8 ? rt.slot(u.pm) : 0;
;         f32x4 cs[2][2];
; #pragma unroll
;         for (int bj = 0; bj < 2; ++bj)
; #pragma unroll
;             for (int n = 0; n < 2; ++n) cs[bj][n] = IN8 ? *(const f32x4*)(cstep + colt + bj * HALF + cl + 4 * n) : (f32x4){1.f, 1.f, 1.f, 1.f};
;         if (u.pn >= gate_tile) {
;             if (wc == 0 && fq < 2) {
; #pragma unroll
;                 for (int ai = 0; ai < 2; ++ai)
; #pragma unroll
;                     for (int m = 0; m < 4; ++m) { const int rl = wr * 64 + ai * HALF + m * 16 + fr; float* gp = G + (size_t)(u.pm * BM + rl) * 16 + 8 * fq;
;                         if (IN8) { const float rs = rt.tab[sl * 256 + rl]; *(f32x4*)gp = i32bits_to_f32(acc[ai][0][m][0]) * cs[0][0] * rs; *(f32x4*)(gp + 4) = i32bits_to_f32(acc[ai][0][m][1]) * cs[0][1] * rs; }
;                         else { *(f32x4*)gp = acc[ai][0][m][0]; *(f32x4*)(gp + 4) = acc[ai][0][m][1]; } }
;             }
;             return;
;         }
; #pragma unroll
;         for (int ai = 0; ai < 2; ++ai)
; #pragma unroll
;             for (int m = 0; m < 4; ++m) { const int rl = wr * 64 + ai * HALF + m * 16 + fr; bf16_t* rowp = O + (size_t)(u.pm * BM + rl) * ldc + colt + cl;
;                 const float rs = IN8 ? rt.tab[sl * 256 + rl] : 1.0f;
; #pragma unroll
;                 for (int bj = 0; bj < 2; ++bj) { f32x4 v0 = acc[ai][bj][m][0], v1 = acc[ai][bj][m][1];
;                     if (IN8) { v0 = i32bits_to_f32(v0) * cs[bj][0] * rs; v1 = i32bits_to_f32(v1) * cs[bj][1] * rs; }
;                     u32x4 w; w.x = cvt_pk_bf16(v0[0], v0[1]); w.y = cvt_pk_bf16(v0[2], v0[3]); w.z = cvt_pk_bf16(v1[0], v1[1]); w.w = cvt_pk_bf16(v1[2], v1[3]);
;                     *(u32x4*)(rowp + bj * HALF) = w; } }
.LBB0_1416:
	s_lshl_b32 s24, s63, 8
	s_ashr_i32 s25, s24, 31
	v_lshl_add_u64 v[2:3], s[24:25], 2, v[140:141]
	global_load_dwordx4 v[14:17], v[2:3], off
	global_load_dwordx4 v[10:13], v[2:3], off offset:16
	global_load_dwordx4 v[6:9], v[2:3], off offset:512
	s_nop 0
	global_load_dwordx4 v[2:5], v[2:3], off offset:528
	s_add_i32 s17, s34, 0x20204
	s_add_i32 s26, s34, 0x2020c
	s_add_i32 s27, s34, 0x20214
	s_add_i32 s28, s34, 0x2021c
	v_mov_b32_e32 v178, s17
	v_mov_b32_e32 v180, s26
	v_mov_b32_e32 v182, s27
	v_mov_b32_e32 v184, s28
	ds_read2_b32 v[178:179], v178 offset1:1
	ds_read2_b32 v[180:181], v180 offset1:1
	ds_read2_b32 v[182:183], v182 offset1:1
	ds_read_b32 v188, v184
	s_lshl_b32 s15, s22, 8
	s_waitcnt lgkmcnt(0)
	v_cmp_eq_u32_e32 vcc, s22, v178
	v_mov_b64_e32 v[166:167], s[6:7]
	v_add_u32_e32 v185, s15, v1
	v_cndmask_b32_e64 v178, 0, 1, vcc
	v_cmp_ne_u32_e32 vcc, s22, v179
	v_add_u32_e32 v186, s15, v169
	v_mad_i64_i32 v[184:185], s[26:27], v185, s62, v[166:167]
	v_cndmask_b32_e32 v178, 2, v178, vcc
	v_cmp_ne_u32_e32 vcc, s22, v180
	s_lshl_b64 s[24:25], s[24:25], 1
	v_mad_i64_i32 v[186:187], s[26:27], v186, s62, v[166:167]
	v_cndmask_b32_e32 v178, 3, v178, vcc
	v_cmp_ne_u32_e32 vcc, s22, v181
	v_lshl_add_u64 v[180:181], v[184:185], 0, s[24:25]
	v_lshl_add_u64 v[180:181], v[180:181], 0, v[138:139]
	v_cndmask_b32_e32 v178, 4, v178, vcc
	v_cmp_ne_u32_e32 vcc, s22, v182
	s_waitcnt vmcnt(0)
	v_pk_mul_f32 v[126:127], v[16:17], v[126:127]
	v_cndmask_b32_e32 v178, 5, v178, vcc
	v_cmp_ne_u32_e32 vcc, s22, v183
	v_pk_mul_f32 v[150:151], v[14:15], v[150:151]
	v_pk_mul_f32 v[124:125], v[12:13], v[124:125]
	v_cndmask_b32_e32 v178, 6, v178, vcc
	v_cmp_ne_u32_e32 vcc, s22, v188
	v_pk_mul_f32 v[122:123], v[10:11], v[122:123]
	v_lshl_add_u64 v[182:183], v[186:187], 0, s[24:25]
	v_cndmask_b32_e32 v178, 7, v178, vcc
	v_pk_mul_f32 v[160:161], v[8:9], v[160:161]
	v_readfirstlane_b32 s17, v178
	v_pk_mul_f32 v[158:159], v[6:7], v[158:159]
	v_pk_mul_f32 v[164:165], v[4:5], v[164:165]
	v_lshl_add_u32 v188, s17, 10, v176
	ds_read2_b32 v[178:179], v188 offset1:16
	ds_read2_b32 v[228:229], v188 offset0:32 offset1:48
	ds_read2_b32 v[230:231], v188 offset0:128 offset1:144
	ds_read2_b32 v[232:233], v188 offset0:160 offset1:176
	v_pk_mul_f32 v[162:163], v[2:3], v[162:163]
	v_pk_mul_f32 v[128:129], v[10:11], v[128:129]
	v_pk_mul_f32 v[120:121], v[8:9], v[120:121]
	v_pk_mul_f32 v[116:117], v[6:7], v[116:117]
	s_waitcnt lgkmcnt(0)
	v_pk_mul_f32 v[126:127], v[126:127], v[178:179] op_sel_hi:[1,0]
	v_pk_mul_f32 v[150:151], v[150:151], v[178:179] op_sel_hi:[1,0]
	v_pk_mul_f32 v[186:187], v[124:125], v[178:179] op_sel_hi:[1,0]
	v_pk_mul_f32 v[124:125], v[122:123], v[178:179] op_sel_hi:[1,0]
	v_mov_b32_e32 v184, v179
	v_pk_mul_f32 v[160:161], v[160:161], v[178:179] op_sel_hi:[1,0]
	v_pk_mul_f32 v[158:159], v[158:159], v[178:179] op_sel_hi:[1,0]
	v_pk_mul_f32 v[164:165], v[164:165], v[178:179] op_sel_hi:[1,0]
	v_pk_mul_f32 v[162:163], v[162:163], v[178:179] op_sel_hi:[1,0]
	v_cvt_pk_bf16_f32 v122, v150, v151
	v_cvt_pk_bf16_f32 v123, v126, v127
	v_cvt_pk_bf16_f32 v124, v124, v125
	v_cvt_pk_bf16_f32 v125, v186, v187
	v_pk_mul_f32 v[118:119], v[4:5], v[118:119]
	v_pk_mul_f32 v[114:115], v[2:3], v[114:115]
	v_pk_mul_f32 v[178:179], v[128:129], v[184:185] op_sel_hi:[1,0]
	v_cvt_pk_bf16_f32 v126, v158, v159
	v_cvt_pk_bf16_f32 v127, v160, v161
	v_cvt_pk_bf16_f32 v128, v162, v163
	v_cvt_pk_bf16_f32 v129, v164, v165
	global_store_dwordx4 v[180:181], v[122:125], off
	global_store_dwordx4 v[180:181], v[126:129], off offset:256
	v_pk_mul_f32 v[120:121], v[120:121], v[184:185] op_sel_hi:[1,0]
	v_pk_mul_f32 v[116:117], v[116:117], v[184:185] op_sel_hi:[1,0]
	v_pk_mul_f32 v[118:119], v[118:119], v[184:185] op_sel_hi:[1,0]
	v_pk_mul_f32 v[122:123], v[114:115], v[184:185] op_sel_hi:[1,0]
	v_lshl_add_u64 v[182:183], v[182:183], 0, v[138:139]
	v_cvt_pk_bf16_f32 v114, v116, v117
	v_cvt_pk_bf16_f32 v115, v120, v121
	v_cvt_pk_bf16_f32 v116, v122, v123
	v_cvt_pk_bf16_f32 v117, v118, v119
	global_store_dwordx4 v[182:183], v[114:117], off offset:256
	s_nop 0
	v_pk_mul_f32 v[104:105], v[16:17], v[104:105]
	v_add_u32_e32 v114, s15, v170
	v_mad_i64_i32 v[114:115], s[26:27], v114, s62, v[166:167]
	v_pk_mul_f32 v[102:103], v[14:15], v[102:103]
	v_pk_mul_f32 v[100:101], v[12:13], v[100:101]
	v_pk_mul_f32 v[98:99], v[10:11], v[98:99]
	v_lshl_add_u64 v[114:115], v[114:115], 0, s[24:25]
	s_waitcnt lgkmcnt(0)
; __device__ __forceinline__ f32x4 i32bits_to_f32(f32x4 v) { return (f32x4){(float)__float_as_int(v.x), (float)__float_as_int(v.y), (float)__float_as_int(v.z), (float)__float_as_int(v.w)}; }
;     __device__ __forceinline__ void operator()(const f32x4 (&acc)[2][2][4][2], const Unit& u, int wr, int wc, int fr, int fq) const {
;     ...
;         for (int ai = 0; ai < 2; ++ai)
; #pragma unroll
;             for (int m = 0; m < 4; ++m) { const int rl = wr * 64 + ai * HALF + m * 16 + fr; bf16_t* rowp = O + (size_t)(u.pm * BM + rl) * ldc + colt + cl;
;                 const float rs = IN8 ? rt.tab[sl * 256 + rl] : 1.0f;
; #pragma unroll
;                 for (int bj = 0; bj < 2; ++bj) { f32x4 v0 = acc[ai][bj][m][0], v1 = acc[ai][bj][m][1];
;                     if (IN8) { v0 = i32bits_to_f32(v0) * cs[bj][0] * rs; v1 = i32bits_to_f32(v1) * cs[bj][1] * rs; }
;                     u32x4 w; w.x = cvt_pk_bf16(v0[0], v0[1]); w.y = cvt_pk_bf16(v0[2], v0[3]); w.z = cvt_pk_bf16(v1[0], v1[1]); w.w = cvt_pk_bf16(v1[2], v1[3]);
;                     *(u32x4*)(rowp + bj * HALF) = w; } }
	v_pk_mul_f32 v[104:105], v[104:105], v[228:229] op_sel_hi:[1,0]
	v_pk_mul_f32 v[102:103], v[102:103], v[228:229] op_sel_hi:[1,0]
	v_pk_mul_f32 v[118:119], v[100:101], v[228:229] op_sel_hi:[1,0]
	v_pk_mul_f32 v[100:101], v[98:99], v[228:229] op_sel_hi:[1,0]
	v_lshl_add_u64 v[114:115], v[114:115], 0, v[138:139]
	v_cvt_pk_bf16_f32 v98, v102, v103
	v_cvt_pk_bf16_f32 v99, v104, v105
	v_cvt_pk_bf16_f32 v100, v100, v101
	v_cvt_pk_bf16_f32 v101, v118, v119
	global_store_dwordx4 v[114:115], v[98:101], off
	v_pk_mul_f32 v[104:105], v[2:3], v[106:107]
	v_pk_mul_f32 v[80:81], v[16:17], v[80:81]
	v_pk_mul_f32 v[98:99], v[8:9], v[112:113]
	v_pk_mul_f32 v[100:101], v[6:7], v[108:109]
	v_pk_mul_f32 v[102:103], v[98:99], v[228:229] op_sel_hi:[1,0]
	v_pk_mul_f32 v[98:99], v[100:101], v[228:229] op_sel_hi:[1,0]
	v_pk_mul_f32 v[100:101], v[4:5], v[110:111]
	v_cvt_pk_bf16_f32 v98, v98, v99
	v_pk_mul_f32 v[106:107], v[100:101], v[228:229] op_sel_hi:[1,0]
	v_pk_mul_f32 v[100:101], v[104:105], v[228:229] op_sel_hi:[1,0]
	v_cvt_pk_bf16_f32 v99, v102, v103
	v_cvt_pk_bf16_f32 v100, v100, v101
	v_cvt_pk_bf16_f32 v101, v106, v107
	global_store_dwordx4 v[114:115], v[98:101], off offset:256
	v_pk_mul_f32 v[76:77], v[14:15], v[76:77]
	v_pk_mul_f32 v[78:79], v[12:13], v[78:79]
	v_add_u32_e32 v98, s15, v171
	v_mad_i64_i32 v[98:99], s[26:27], v98, s62, v[166:167]
	v_mov_b32_e32 v100, v229
	v_pk_mul_f32 v[74:75], v[10:11], v[74:75]
	v_lshl_add_u64 v[98:99], v[98:99], 0, s[24:25]
	v_pk_mul_f32 v[80:81], v[80:81], v[100:101] op_sel_hi:[1,0]
	v_pk_mul_f32 v[76:77], v[76:77], v[100:101] op_sel_hi:[1,0]
	v_pk_mul_f32 v[78:79], v[78:79], v[100:101] op_sel_hi:[1,0]
	v_pk_mul_f32 v[102:103], v[74:75], v[100:101] op_sel_hi:[1,0]
	v_lshl_add_u64 v[98:99], v[98:99], 0, v[138:139]
	v_cvt_pk_bf16_f32 v74, v76, v77
	v_cvt_pk_bf16_f32 v75, v80, v81
	v_cvt_pk_bf16_f32 v76, v102, v103
	v_cvt_pk_bf16_f32 v77, v78, v79
	global_store_dwordx4 v[98:99], v[74:77], off
	v_pk_mul_f32 v[80:81], v[2:3], v[90:91]
	v_pk_mul_f32 v[72:73], v[16:17], v[72:73]
	v_pk_mul_f32 v[74:75], v[8:9], v[96:97]
	v_pk_mul_f32 v[76:77], v[6:7], v[92:93]
	v_pk_mul_f32 v[78:79], v[74:75], v[100:101] op_sel_hi:[1,0]
	v_pk_mul_f32 v[74:75], v[76:77], v[100:101] op_sel_hi:[1,0]
	v_pk_mul_f32 v[76:77], v[4:5], v[94:95]
	v_cvt_pk_bf16_f32 v74, v74, v75
	v_pk_mul_f32 v[90:91], v[76:77], v[100:101] op_sel_hi:[1,0]
	v_pk_mul_f32 v[76:77], v[80:81], v[100:101] op_sel_hi:[1,0]
	v_cvt_pk_bf16_f32 v75, v78, v79
	v_cvt_pk_bf16_f32 v76, v76, v77
	v_cvt_pk_bf16_f32 v77, v90, v91
	global_store_dwordx4 v[98:99], v[74:77], off offset:256
	s_nop 0
	v_pk_mul_f32 v[68:69], v[14:15], v[68:69]
	v_add_u32_e32 v74, s15, v172
	v_mad_i64_i32 v[74:75], s[26:27], v74, s62, v[166:167]
	v_pk_mul_f32 v[70:71], v[12:13], v[70:71]
	v_pk_mul_f32 v[66:67], v[10:11], v[66:67]
	v_lshl_add_u64 v[74:75], v[74:75], 0, s[24:25]
	s_waitcnt lgkmcnt(0)
; __device__ __forceinline__ f32x4 i32bits_to_f32(f32x4 v) { return (f32x4){(float)__float_as_int(v.x), (float)__float_as_int(v.y), (float)__float_as_int(v.z), (float)__float_as_int(v.w)}; }
;     __device__ __forceinline__ void operator()(const f32x4 (&acc)[2][2][4][2], const Unit& u, int wr, int wc, int fr, int fq) const {
;     ...
;         for (int ai = 0; ai < 2; ++ai)
; #pragma unroll
;             for (int m = 0; m < 4; ++m) { const int rl = wr * 64 + ai * HALF + m * 16 + fr; bf16_t* rowp = O + (size_t)(u.pm * BM + rl) * ldc + colt + cl;
;                 const float rs = IN8 ? rt.tab[sl * 256 + rl] : 1.0f;
; #pragma unroll
;                 for (int bj = 0; bj < 2; ++bj) { f32x4 v0 = acc[ai][bj][m][0], v1 = acc[ai][bj][m][1];
;                     if (IN8) { v0 = i32bits_to_f32(v0) * cs[bj][0] * rs; v1 = i32bits_to_f32(v1) * cs[bj][1] * rs; }
;                     u32x4 w; w.x = cvt_pk_bf16(v0[0], v0[1]); w.y = cvt_pk_bf16(v0[2], v0[3]); w.z = cvt_pk_bf16(v1[0], v1[1]); w.w = cvt_pk_bf16(v1[2], v1[3]);
;                     *(u32x4*)(rowp + bj * HALF) = w; } }
	v_pk_mul_f32 v[72:73], v[72:73], v[230:231] op_sel_hi:[1,0]
	v_pk_mul_f32 v[68:69], v[68:69], v[230:231] op_sel_hi:[1,0]
	v_pk_mul_f32 v[70:71], v[70:71], v[230:231] op_sel_hi:[1,0]
	v_pk_mul_f32 v[78:79], v[66:67], v[230:231] op_sel_hi:[1,0]
	v_lshl_add_u64 v[74:75], v[74:75], 0, v[138:139]
	v_cvt_pk_bf16_f32 v66, v68, v69
	v_cvt_pk_bf16_f32 v67, v72, v73
	v_cvt_pk_bf16_f32 v68, v78, v79
	v_cvt_pk_bf16_f32 v69, v70, v71
	global_store_dwordx4 v[74:75], v[66:69], off
	v_pk_mul_f32 v[72:73], v[2:3], v[82:83]
	v_pk_mul_f32 v[154:155], v[16:17], v[154:155]
	v_pk_mul_f32 v[66:67], v[8:9], v[88:89]
	v_pk_mul_f32 v[68:69], v[6:7], v[84:85]
	v_pk_mul_f32 v[70:71], v[66:67], v[230:231] op_sel_hi:[1,0]
	v_pk_mul_f32 v[66:67], v[68:69], v[230:231] op_sel_hi:[1,0]
	v_pk_mul_f32 v[68:69], v[4:5], v[86:87]
	v_cvt_pk_bf16_f32 v66, v66, v67
	v_pk_mul_f32 v[78:79], v[68:69], v[230:231] op_sel_hi:[1,0]
	v_pk_mul_f32 v[68:69], v[72:73], v[230:231] op_sel_hi:[1,0]
	v_cvt_pk_bf16_f32 v67, v70, v71
	v_cvt_pk_bf16_f32 v68, v68, v69
	v_cvt_pk_bf16_f32 v69, v78, v79
	global_store_dwordx4 v[74:75], v[66:69], off offset:256
	v_pk_mul_f32 v[152:153], v[14:15], v[152:153]
	v_pk_mul_f32 v[156:157], v[12:13], v[156:157]
	v_add_u32_e32 v66, s15, v173
	v_mad_i64_i32 v[66:67], s[26:27], v66, s62, v[166:167]
	v_pk_mul_f32 v[56:57], v[16:17], v[56:57]
	v_pk_mul_f32 v[54:55], v[14:15], v[54:55]
	v_mov_b32_e32 v68, v231
	v_pk_mul_f32 v[52:53], v[12:13], v[52:53]
	v_pk_mul_f32 v[50:51], v[10:11], v[50:51]
	v_pk_mul_f32 v[154:155], v[154:155], v[184:185] op_sel_hi:[1,0]
	v_pk_mul_f32 v[152:153], v[152:153], v[184:185] op_sel_hi:[1,0]
	v_pk_mul_f32 v[156:157], v[156:157], v[184:185] op_sel_hi:[1,0]
	v_lshl_add_u64 v[66:67], v[66:67], 0, s[24:25]
	v_pk_mul_f32 v[56:57], v[56:57], v[68:69] op_sel_hi:[1,0]
	v_pk_mul_f32 v[54:55], v[54:55], v[68:69] op_sel_hi:[1,0]
	v_pk_mul_f32 v[70:71], v[52:53], v[68:69] op_sel_hi:[1,0]
	v_pk_mul_f32 v[52:53], v[50:51], v[68:69] op_sel_hi:[1,0]
	v_cvt_pk_bf16_f32 v150, v152, v153
	v_cvt_pk_bf16_f32 v151, v154, v155
	v_cvt_pk_bf16_f32 v152, v178, v179
	v_cvt_pk_bf16_f32 v153, v156, v157
	v_lshl_add_u64 v[66:67], v[66:67], 0, v[138:139]
	v_cvt_pk_bf16_f32 v50, v54, v55
	v_cvt_pk_bf16_f32 v51, v56, v57
	v_cvt_pk_bf16_f32 v52, v52, v53
	v_cvt_pk_bf16_f32 v53, v70, v71
	global_store_dwordx4 v[182:183], v[150:153], off
	global_store_dwordx4 v[66:67], v[50:53], off
	v_pk_mul_f32 v[56:57], v[2:3], v[58:59]
	v_pk_mul_f32 v[40:41], v[16:17], v[40:41]
	v_pk_mul_f32 v[50:51], v[8:9], v[64:65]
	v_pk_mul_f32 v[52:53], v[6:7], v[60:61]
	v_pk_mul_f32 v[54:55], v[50:51], v[68:69] op_sel_hi:[1,0]
	v_pk_mul_f32 v[50:51], v[52:53], v[68:69] op_sel_hi:[1,0]
	v_pk_mul_f32 v[52:53], v[4:5], v[62:63]
	v_cvt_pk_bf16_f32 v50, v50, v51
	v_pk_mul_f32 v[58:59], v[52:53], v[68:69] op_sel_hi:[1,0]
	v_pk_mul_f32 v[52:53], v[56:57], v[68:69] op_sel_hi:[1,0]
	v_cvt_pk_bf16_f32 v51, v54, v55
	v_cvt_pk_bf16_f32 v52, v52, v53
	v_cvt_pk_bf16_f32 v53, v58, v59
	global_store_dwordx4 v[66:67], v[50:53], off offset:256
	s_nop 0
	v_pk_mul_f32 v[38:39], v[14:15], v[38:39]
	v_add_u32_e32 v50, s15, v174
	v_mad_i64_i32 v[50:51], s[26:27], v50, s62, v[166:167]
	v_pk_mul_f32 v[36:37], v[12:13], v[36:37]
	v_pk_mul_f32 v[34:35], v[10:11], v[34:35]
	v_lshl_add_u64 v[50:51], v[50:51], 0, s[24:25]
	s_waitcnt lgkmcnt(0)
	v_pk_mul_f32 v[40:41], v[40:41], v[232:233] op_sel_hi:[1,0]
	v_pk_mul_f32 v[38:39], v[38:39], v[232:233] op_sel_hi:[1,0]
	v_pk_mul_f32 v[54:55], v[36:37], v[232:233] op_sel_hi:[1,0]
	v_pk_mul_f32 v[36:37], v[34:35], v[232:233] op_sel_hi:[1,0]
	v_lshl_add_u64 v[50:51], v[50:51], 0, v[138:139]
	v_cvt_pk_bf16_f32 v34, v38, v39
	v_cvt_pk_bf16_f32 v35, v40, v41
	v_cvt_pk_bf16_f32 v36, v36, v37
	v_cvt_pk_bf16_f32 v37, v54, v55
	global_store_dwordx4 v[50:51], v[34:37], off
	v_pk_mul_f32 v[40:41], v[2:3], v[42:43]
	v_pk_mul_f32 v[16:17], v[16:17], v[24:25]
	v_pk_mul_f32 v[34:35], v[8:9], v[48:49]
	v_pk_mul_f32 v[36:37], v[6:7], v[44:45]
	v_pk_mul_f32 v[38:39], v[34:35], v[232:233] op_sel_hi:[1,0]
	v_pk_mul_f32 v[34:35], v[36:37], v[232:233] op_sel_hi:[1,0]
	v_pk_mul_f32 v[36:37], v[4:5], v[46:47]
	v_cvt_pk_bf16_f32 v34, v34, v35
	v_pk_mul_f32 v[42:43], v[36:37], v[232:233] op_sel_hi:[1,0]
	v_pk_mul_f32 v[36:37], v[40:41], v[232:233] op_sel_hi:[1,0]
	v_cvt_pk_bf16_f32 v35, v38, v39
	v_cvt_pk_bf16_f32 v36, v36, v37
	v_cvt_pk_bf16_f32 v37, v42, v43
	global_store_dwordx4 v[50:51], v[34:37], off offset:256
	v_pk_mul_f32 v[14:15], v[14:15], v[22:23]
	v_mov_b32_e32 v22, v233
	v_add_u32_e32 v34, s15, v175
	v_mad_i64_i32 v[34:35], s[26:27], v34, s62, v[166:167]
	v_pk_mul_f32 v[12:13], v[12:13], v[20:21]
	v_pk_mul_f32 v[10:11], v[10:11], v[18:19]
	v_lshl_add_u64 v[34:35], v[34:35], 0, s[24:25]
	v_pk_mul_f32 v[16:17], v[16:17], v[22:23] op_sel_hi:[1,0]
	v_pk_mul_f32 v[14:15], v[14:15], v[22:23] op_sel_hi:[1,0]
	v_pk_mul_f32 v[18:19], v[12:13], v[22:23] op_sel_hi:[1,0]
	v_pk_mul_f32 v[12:13], v[10:11], v[22:23] op_sel_hi:[1,0]
	v_lshl_add_u64 v[34:35], v[34:35], 0, v[138:139]
	v_cvt_pk_bf16_f32 v10, v14, v15
	v_cvt_pk_bf16_f32 v11, v16, v17
	v_cvt_pk_bf16_f32 v12, v12, v13
	v_cvt_pk_bf16_f32 v13, v18, v19
	v_pk_mul_f32 v[8:9], v[8:9], v[32:33]
	v_pk_mul_f32 v[6:7], v[6:7], v[28:29]
	v_pk_mul_f32 v[4:5], v[4:5], v[30:31]
	v_pk_mul_f32 v[2:3], v[2:3], v[26:27]
	global_store_dwordx4 v[34:35], v[10:13], off
	v_pk_mul_f32 v[8:9], v[8:9], v[22:23] op_sel_hi:[1,0]
	v_pk_mul_f32 v[6:7], v[6:7], v[22:23] op_sel_hi:[1,0]
	v_pk_mul_f32 v[10:11], v[4:5], v[22:23] op_sel_hi:[1,0]
	v_pk_mul_f32 v[4:5], v[2:3], v[22:23] op_sel_hi:[1,0]
	v_cvt_pk_bf16_f32 v2, v6, v7
	v_cvt_pk_bf16_f32 v3, v8, v9
	v_cvt_pk_bf16_f32 v4, v4, v5
	v_cvt_pk_bf16_f32 v5, v10, v11
	s_andn2_b64 vcc, exec, s[0:1]
	s_mov_b64 s[0:1], -1
	global_store_dwordx4 v[34:35], v[2:5], off offset:256
	s_cbranch_vccnz .LBB0_1407
	s_andn2_b64 vcc, exec, s[4:5]
	s_cbranch_vccnz .LBB0_1406
	s_barrier
	s_branch .LBB0_1406
